# baseline (speedup 1.0000x reference)
_Z15k_scatter_gemm1PKiS0_PiPjPyPKfPK6__halfS5_S5_PS6_PfSA_:
	s_cmpk_gt_u32 s2, 0x186
	s_mov_b64 s[4:5], -1
	s_cbranch_scc0 .LBB1_22
	s_load_dwordx2 s[26:27], s[0:1], 0x28
	s_load_dwordx2 s[10:11], s[0:1], 0x30
	s_load_dwordx4 s[28:31], s[0:1], 0x38
	v_lshlrev_b32_e32 v92, 4, v0
	v_add_u32_e32 v93, 0x1000, v92
	v_add_u32_e32 v94, 0x2000, v92
	v_add_u32_e32 v95, 0x3000, v92
	v_add_u32_e32 v96, 0x4000, v92
	v_add_u32_e32 v97, 0x5000, v92
	v_add_u32_e32 v98, 0x6000, v92
	v_add_u32_e32 v99, 0x7000, v92
	v_add_u32_e32 v100, 0x8000, v92
	v_lshlrev_b32_e32 v101, 2, v0
	s_movk_i32 s3, 0x80
	v_cmp_gt_u32_e64 s[8:9], s3, v0
	s_waitcnt lgkmcnt(0)
	global_load_dwordx4 v[104:107], v92, s[10:11]
	global_load_dwordx4 v[108:111], v93, s[10:11]
	global_load_dwordx4 v[112:115], v94, s[10:11]
	global_load_dwordx4 v[116:119], v95, s[10:11]
	global_load_dwordx4 v[120:123], v96, s[10:11]
	global_load_dwordx4 v[124:127], v97, s[10:11]
	global_load_dwordx4 v[128:131], v98, s[10:11]
	global_load_dwordx4 v[132:135], v99, s[10:11]
	s_and_saveexec_b64 s[4:5], s[8:9]
	global_load_dwordx4 v[136:139], v100, s[10:11]
	global_load_dword v140, v101, s[28:29]
	global_load_dword v141, v101, s[30:31]
	s_mov_b64 exec, s[4:5]
	s_lshl_b32 s3, s2, 2
	v_lshrrev_b32_e32 v14, 6, v0
	s_add_i32 s4, s3, 0xfffff9e4
	v_or_b32_e32 v2, s4, v14
	s_movk_i32 s4, 2500
	v_cmp_gt_i32_e32 vcc, s4, v2
	v_and_b32_e32 v1, 15, v0
	v_and_b32_e32 v66, 48, v0
	v_mov_b32_e32 v67, 0
	s_and_saveexec_b64 s[6:7], vcc
	s_cbranch_execz .Lg1_noval
	v_lshl_or_b32 v2, v2, 4, v1
	v_ashrrev_i32_e32 v3, 31, v2
	v_lshlrev_b64 v[2:3], 9, v[2:3]
	v_lshl_add_u64 v[2:3], s[26:27], 0, v[2:3]
	v_lshl_add_u64 v[16:17], v[2:3], 0, v[66:67]
	global_load_dwordx4 v[38:41], v[16:17], off offset:448 nt
	global_load_dwordx4 v[34:37], v[16:17], off offset:384 nt
	global_load_dwordx4 v[46:49], v[16:17], off offset:320 nt
	global_load_dwordx4 v[42:45], v[16:17], off offset:256 nt
	global_load_dwordx4 v[6:9], v[16:17], off offset:192 nt
	global_load_dwordx4 v[18:21], v[16:17], off offset:128 nt
	global_load_dwordx4 v[2:5], v[16:17], off offset:64 nt
	global_load_dwordx4 v[10:13], v[16:17], off nt
	s_mov_b64 exec, s[6:7]
	s_waitcnt vmcnt(8)
	s_branch .Lg1_stage

.LBB1_19:
	ds_read_b128 v[14:17], v83
	v_cvt_pk_f16_f32 v5, v4, v5
	v_cvt_pk_f16_f32 v4, v2, v3
	v_cvt_pk_f16_f32 v3, v12, v13
	v_cvt_pk_f16_f32 v2, v10, v11
	ds_read_b128 v[10:13], v83 offset:64
	ds_read_b128 v[22:25], v83 offset:4352
	ds_read_b128 v[26:29], v83 offset:4416
	ds_read_b128 v[30:33], v83 offset:8704
	ds_read_b128 v[50:53], v83 offset:8768
	ds_read_b128 v[54:57], v83 offset:13056
	ds_read_b128 v[58:61], v83 offset:13120
	ds_read_b128 v[62:65], v83 offset:17408
	ds_read_b128 v[72:75], v83 offset:17472
	ds_read_b128 v[76:79], v83 offset:21760
	ds_read_b128 v[92:95], v83 offset:21824
	ds_read_b128 v[96:99], v83 offset:26112
	ds_read_b128 v[100:103], v83 offset:26176
	ds_read_b128 v[104:107], v83 offset:30464
	ds_read_b128 v[110:113], v83 offset:30528
	v_add_u32_e32 v91, 0xfffffa1c, v67
	v_cmp_gt_i32_e64 s[4:5], s3, v91
	s_mov_b64 s[36:37], s[4:5]
	s_waitcnt lgkmcnt(14)
	v_mfma_f32_16x16x32_f16 v[14:17], v[14:17], v[2:5], 0
	v_cvt_pk_f16_f32 v109, v8, v9
	v_cvt_pk_f16_f32 v108, v6, v7
	v_cvt_pk_f16_f32 v49, v48, v49
	s_waitcnt lgkmcnt(13)
	v_mfma_f32_16x16x32_f16 v[22:25], v[22:25], v[2:5], 0
	v_cvt_pk_f16_f32 v48, v46, v47
	v_cvt_pk_f16_f32 v47, v44, v45
	v_cvt_pk_f16_f32 v46, v42, v43
	s_waitcnt lgkmcnt(11)
	v_mfma_f32_16x16x32_f16 v[30:33], v[30:33], v[2:5], 0
	s_waitcnt lgkmcnt(9)
	v_mfma_f32_16x16x32_f16 v[54:57], v[54:57], v[2:5], 0
	s_waitcnt lgkmcnt(7)
	v_mfma_f32_16x16x32_f16 v[62:65], v[62:65], v[2:5], 0
	s_waitcnt lgkmcnt(5)
	v_mfma_f32_16x16x32_f16 v[76:79], v[76:79], v[2:5], 0
	s_waitcnt lgkmcnt(3)
	v_mfma_f32_16x16x32_f16 v[96:99], v[96:99], v[2:5], 0
	s_waitcnt lgkmcnt(1)
	v_mfma_f32_16x16x32_f16 v[114:117], v[104:107], v[2:5], 0
	v_cndmask_b32_e64 v2, v91, v67, s[4:5]
	v_lshl_or_b32 v2, v2, 4, v1
	v_ashrrev_i32_e32 v3, 31, v2
	v_cvt_pk_f16_f32 v107, v20, v21
	v_cvt_pk_f16_f32 v106, v18, v19
	v_lshlrev_b64 v[2:3], 9, v[2:3]
	v_cmp_lt_i32_e64 s[4:5], v85, v86
	v_mfma_f32_16x16x32_f16 v[122:125], v[26:29], v[106:109], v[22:25]
	s_nop 2
	v_lshl_add_u64 v[22:23], v[68:69], 0, v[2:3]
	v_mfma_f32_16x16x32_f16 v[118:121], v[10:13], v[106:109], v[14:17]
	s_cmp_eq_u64 s[36:37], 0
	s_cbranch_scc1 .Lg1_nopfA
	global_load_dwordx4 v[10:13], v[22:23], off nt
	global_load_dwordx4 v[2:5], v[22:23], off offset:64 nt
	global_load_dwordx4 v[18:21], v[22:23], off offset:128 nt
	global_load_dwordx4 v[6:9], v[22:23], off offset:192 nt
	global_load_dwordx4 v[26:29], v[22:23], off offset:256 nt
	global_load_dwordx4 v[14:17], v[22:23], off offset:320 nt
.Lg1_nopfA:
	v_mfma_f32_16x16x32_f16 v[50:53], v[50:53], v[106:109], v[30:33]
	s_nop 2
	s_cmp_eq_u64 s[36:37], 0
	s_cbranch_scc1 .Lg1_nopfB
	global_load_dwordx4 v[30:33], v[22:23], off offset:384 nt
	s_nop 0
	global_load_dwordx4 v[22:25], v[22:23], off offset:448 nt

_Z12k_fine_gemm1PKjPKyPKiPiS5_S5_S5_PKfPK6__halfS7_S7_PS8_PfSC_:
	s_cmpk_gt_u32 s2, 0x186
	s_mov_b64 s[4:5], -1
	s_cbranch_scc0 .LBB2_22
	s_load_dwordx2 s[26:27], s[0:1], 0x38
	s_load_dwordx2 s[10:11], s[0:1], 0x40
	s_load_dwordx4 s[28:31], s[0:1], 0x48
	v_lshlrev_b32_e32 v92, 4, v0
	v_add_u32_e32 v93, 0x1000, v92
	v_add_u32_e32 v94, 0x2000, v92
	v_add_u32_e32 v95, 0x3000, v92
	v_add_u32_e32 v96, 0x4000, v92
	v_add_u32_e32 v97, 0x5000, v92
	v_add_u32_e32 v98, 0x6000, v92
	v_add_u32_e32 v99, 0x7000, v92
	v_add_u32_e32 v100, 0x8000, v92
	v_lshlrev_b32_e32 v101, 2, v0
	s_movk_i32 s3, 0x80
	v_cmp_gt_u32_e64 s[8:9], s3, v0
	s_waitcnt lgkmcnt(0)
	global_load_dwordx4 v[104:107], v92, s[10:11]
	global_load_dwordx4 v[108:111], v93, s[10:11]
	global_load_dwordx4 v[112:115], v94, s[10:11]
	global_load_dwordx4 v[116:119], v95, s[10:11]
	global_load_dwordx4 v[120:123], v96, s[10:11]
	global_load_dwordx4 v[124:127], v97, s[10:11]
	global_load_dwordx4 v[128:131], v98, s[10:11]
	global_load_dwordx4 v[132:135], v99, s[10:11]
	s_and_saveexec_b64 s[4:5], s[8:9]
	global_load_dwordx4 v[136:139], v100, s[10:11]
	global_load_dword v140, v101, s[28:29]
	global_load_dword v141, v101, s[30:31]
	s_mov_b64 exec, s[4:5]
	s_lshl_b32 s3, s2, 2
	v_lshrrev_b32_e32 v14, 6, v0
	s_addk_i32 s3, 936
	v_add_u32_e32 v1, s3, v14
	s_movk_i32 s3, 0x186a
	v_cmp_gt_i32_e32 vcc, s3, v1
	v_and_b32_e32 v80, 15, v0
	v_and_b32_e32 v66, 48, v0
	v_mov_b32_e32 v67, 0
	s_and_saveexec_b64 s[6:7], vcc
	s_cbranch_execz .Lg2_noval
	v_lshl_or_b32 v2, v1, 4, v80
	v_ashrrev_i32_e32 v3, 31, v2
	v_lshlrev_b64 v[2:3], 9, v[2:3]
	v_lshl_add_u64 v[2:3], s[26:27], 0, v[2:3]
	v_lshl_add_u64 v[16:17], v[2:3], 0, v[66:67]
	global_load_dwordx4 v[38:41], v[16:17], off offset:448 nt
	global_load_dwordx4 v[34:37], v[16:17], off offset:384 nt
	global_load_dwordx4 v[26:29], v[16:17], off offset:320 nt
	global_load_dwordx4 v[30:33], v[16:17], off offset:256 nt
	global_load_dwordx4 v[6:9], v[16:17], off offset:192 nt
	global_load_dwordx4 v[18:21], v[16:17], off offset:128 nt
	global_load_dwordx4 v[2:5], v[16:17], off offset:64 nt
	global_load_dwordx4 v[10:13], v[16:17], off nt
	s_mov_b64 exec, s[6:7]
	s_waitcnt vmcnt(8)
	s_branch .Lg2_stage

.LBB2_19:
	ds_read_b128 v[14:17], v83
	v_cvt_pk_f16_f32 v5, v4, v5
	v_cvt_pk_f16_f32 v4, v2, v3
	v_cvt_pk_f16_f32 v3, v12, v13
	v_cvt_pk_f16_f32 v2, v10, v11
	ds_read_b128 v[10:13], v83 offset:64
	ds_read_b128 v[22:25], v83 offset:4352
	ds_read_b128 v[42:45], v83 offset:4416
	ds_read_b128 v[46:49], v83 offset:8704
	ds_read_b128 v[50:53], v83 offset:8768
	ds_read_b128 v[54:57], v83 offset:13056
	ds_read_b128 v[58:61], v83 offset:13120
	ds_read_b128 v[62:65], v83 offset:17408
	ds_read_b128 v[72:75], v83 offset:17472
	ds_read_b128 v[76:79], v83 offset:21760
	ds_read_b128 v[92:95], v83 offset:21824
	ds_read_b128 v[96:99], v83 offset:26112
	ds_read_b128 v[100:103], v83 offset:26176
	ds_read_b128 v[104:107], v83 offset:30464
	ds_read_b128 v[110:113], v83 offset:30528
	v_mov_b32_e32 v91, v1
	v_add_u32_e32 v1, 0x5e4, v91
	v_cmp_gt_i32_e64 s[4:5], s14, v91
	s_mov_b64 s[36:37], s[4:5]
	s_waitcnt lgkmcnt(14)
	v_mfma_f32_16x16x32_f16 v[14:17], v[14:17], v[2:5], 0
	v_cvt_pk_f16_f32 v109, v8, v9
	v_cvt_pk_f16_f32 v108, v6, v7
	v_cvt_pk_f16_f32 v127, v40, v41
	s_waitcnt lgkmcnt(13)
	v_mfma_f32_16x16x32_f16 v[22:25], v[22:25], v[2:5], 0
	v_cvt_pk_f16_f32 v126, v38, v39
	v_cvt_pk_f16_f32 v125, v36, v37
	v_cvt_pk_f16_f32 v124, v34, v35
	s_waitcnt lgkmcnt(11)
	v_mfma_f32_16x16x32_f16 v[46:49], v[46:49], v[2:5], 0
	s_waitcnt lgkmcnt(9)
	v_mfma_f32_16x16x32_f16 v[54:57], v[54:57], v[2:5], 0
	s_waitcnt lgkmcnt(7)
	v_mfma_f32_16x16x32_f16 v[62:65], v[62:65], v[2:5], 0
	s_waitcnt lgkmcnt(5)
	v_mfma_f32_16x16x32_f16 v[76:79], v[76:79], v[2:5], 0
	s_waitcnt lgkmcnt(3)
	v_mfma_f32_16x16x32_f16 v[96:99], v[96:99], v[2:5], 0
	s_waitcnt lgkmcnt(1)
	v_mfma_f32_16x16x32_f16 v[114:117], v[104:107], v[2:5], 0
	v_cndmask_b32_e64 v2, v91, v1, s[4:5]
	v_lshl_or_b32 v2, v2, 4, v80
	v_ashrrev_i32_e32 v3, 31, v2
	v_lshlrev_b64 v[2:3], 9, v[2:3]
	v_cvt_pk_f16_f32 v107, v20, v21
	v_cvt_pk_f16_f32 v106, v18, v19
	v_lshl_add_u64 v[122:123], v[68:69], 0, v[2:3]
	v_cmp_lt_i32_e64 s[4:5], v85, v86
	v_mfma_f32_16x16x32_f16 v[118:121], v[10:13], v[106:109], v[14:17]
	s_cmp_eq_u64 s[36:37], 0
	s_cbranch_scc1 .Lg2_nopfA
	global_load_dwordx4 v[10:13], v[122:123], off nt
	global_load_dwordx4 v[2:5], v[122:123], off offset:64 nt
	global_load_dwordx4 v[18:21], v[122:123], off offset:128 nt
	global_load_dwordx4 v[6:9], v[122:123], off offset:192 nt
.Lg2_nopfA:
	v_cndmask_b32_e64 v34, v84, v85, s[4:5]
	v_lshlrev_b32_e32 v142, 2, v34
	v_mfma_f32_16x16x32_f16 v[42:45], v[42:45], v[106:109], v[22:25]
	s_nop 2
	s_cmp_eq_u64 s[36:37], 0
	s_cbranch_scc1 .Lg2_nopfB
	global_load_dwordx4 v[22:25], v[122:123], off offset:256 nt
	global_load_dwordx4 v[14:17], v[122:123], off offset:320 nt
.Lg2_nopfB:
	v_cmp_lt_i32_e64 s[4:5], v87, v86
	v_mfma_f32_16x16x32_f16 v[46:49], v[50:53], v[106:109], v[46:49]
	s_nop 0
	v_cndmask_b32_e64 v143, v84, v87, s[4:5]
	v_cmp_lt_i32_e64 s[4:5], s3, v91
	v_mfma_f32_16x16x32_f16 v[50:53], v[58:61], v[106:109], v[54:57]
	v_mfma_f32_16x16x32_f16 v[54:57], v[72:75], v[106:109], v[62:65]
	ds_read_b128 v[72:75], v83 offset:128
	v_mfma_f32_16x16x32_f16 v[58:61], v[92:95], v[106:109], v[76:79]
	s_nop 0
	v_cvt_pk_f16_f32 v65, v28, v29
	v_cvt_pk_f16_f32 v64, v26, v27
	v_cvt_pk_f16_f32 v63, v32, v33
	v_mfma_f32_16x16x32_f16 v[76:79], v[100:103], v[106:109], v[96:99]
	ds_read_b128 v[92:95], v83 offset:4480
	v_cvt_pk_f16_f32 v62, v30, v31
	s_waitcnt lgkmcnt(2)
	v_mfma_f32_16x16x32_f16 v[96:99], v[110:113], v[106:109], v[114:117]
	ds_read_b128 v[100:103], v83 offset:8832
	ds_read_b128 v[104:107], v83 offset:192
	s_cmp_eq_u64 s[36:37], 0
	s_cbranch_scc1 .Lg2_nopfC
	global_load_dwordx4 v[30:33], v[122:123], off offset:384 nt
	global_load_dwordx4 v[26:29], v[122:123], off offset:448 nt
